# as v72 but the MoE-down e4m3 conversion is split: 14 items per wave ride in the attention trips, 14 in the MoE gate/up GEMM epilogues
# speedup vs baseline: 1.0133x; 1.0004x over previous
; #define RP(n) _Pragma("nounroll") for (int rep_ = 0; rep_ < (int)(((REPEAT) >> (n)) & 1u) + 1; ++rep_)
; __global__ void __launch_bounds__(NTHREADS, 2) fwd_kernel(Args args) {
;     ...
;     if (PH(15)) RP(15)
;     {
;         const int vcu = (G % 8 == 0) ? (bx % 8) * (G / 8) + bx / 8 : bx;
;         att::CvtState cs{args.in[I_MOED], ws + W_MOED, gw * att::CV_IPW, (gw + 1) * att::CV_IPW};
;         for (int L = vcu; L < NBATCH * NH * 8; L += G) {
.LBB0_1020:
	s_or_b64 exec, exec, s[4:5]
	s_lshr_b32 s0, s3, 29
	s_add_i32 s5, s2, s0
	s_and_b32 s0, s5, -8
	s_ashr_i32 s1, s76, 3
	s_sub_i32 s0, s2, s0
	s_mul_i32 s8, s1, s0
	s_ashr_i32 s1, s5, 3
	s_and_b32 s4, s76, 7
	s_add_i32 s5, s8, s1
	v_readlane_b32 s8, v251, 9
	s_add_u32 s30, s70, 0x24a00000
	s_mul_i32 s35, s8, 28
	s_addc_u32 s31, s71, 0
	s_add_i32 s50, s35, 14
	v_readlane_b32 s9, v251, 10
	s_add_u32 s8, s70, 0x4bc00000
	s_addc_u32 s9, s71, 0
	s_cmp_eq_u32 s4, 0
	s_cselect_b32 s51, s5, s2
	s_cmpk_gt_i32 s51, 0x1ff
	s_waitcnt lgkmcnt(0)
	s_barrier
	s_cbranch_scc1 .LBB0_1053
	s_add_u32 s4, s70, 0x3da00000
	s_addc_u32 s5, s71, 0
	s_add_u32 s10, s70, 0x3c200000
	s_addc_u32 s11, s71, 0
	s_movk_i32 s52, 0x2000
	s_mov_b32 s53, 0xc3e00000
	v_mov_b32_e32 v203, 0x43e00000
	v_mov_b32_e32 v191, 0
	s_movk_i32 s54, 0xd0
	s_movk_i32 s55, 0x3000
	s_mov_b32 s56, 0x5010400
	s_mov_b32 s57, 0x7030602
	s_mov_b32 s58, 0x5040100
	s_mov_b32 s59, 0x7060302
	s_add_i32 s60, 0, 0x6800
	s_movk_i32 s61, 0x1c00
	s_movk_i32 s62, 0x4000
	s_movk_i32 s63, 0x6000
	s_mov_b32 s64, 0x8000
	s_mov_b32 s65, 0xa000
	s_mov_b32 s66, 0xc000
	s_mov_b32 s67, 0xe000
	v_mov_b32_e32 v208, 0x1c00
	v_mov_b32_e32 v209, 0xff800000
	v_readlane_b32 s18, v251, 0
	v_readlane_b32 s19, v251, 1
	v_readlane_b32 s98, v251, 9
	s_nop 3
	s_sub_u32 s18, s18, 0x38
	s_subb_u32 s19, s19, 0
	s_load_dwordx4 s[44:47], s[18:19], 0x0
	s_mul_i32 s98, s98, 56
	s_add_i32 s99, s98, 56
	s_mov_b32 s100, 0
	s_waitcnt lgkmcnt(0)
	v_writelane_b32 v252, s44, 0
	v_writelane_b32 v252, s45, 1
	v_writelane_b32 v252, s46, 2
	v_writelane_b32 v252, s47, 3
	s_branch .LBB0_1023

; #define LAS __attribute__((address_space(3)))
;     __device__ __forceinline__ bool next(int i, Unit& u) const { if (!T.tile(i, u.pm, u.pn)) return false; u.aoff = (size_t)u.pm * atile; u.boff = (size_t)u.pn * btile; return true; }
;     __device__ __forceinline__ bool next(int i, Unit& u) const { if (!T.tile(i, u.pm, u.pn)) return false; u.aoff = (size_t)u.pm * 256 * D * 2 + (size_t)(u.pn >> 1) * 512; u.boff = (size_t)u.pn * 256 * 256 * 2; return true; }
; #define PG8_WAIT_V(n) asm volatile("s_waitcnt vmcnt(" #n ")" ::: "memory")
;     ...
;     PG8_STAGE(PG8_SB(0, 0), cB, voffB); PG8_STAGE(PG8_SB(0, 1), cB + hstepB, voffB); PG8_STAGE(PG8_SA(0, 0), cA, voffA); PG8_STAGE(PG8_SA(0, 1), cA + hstepA, voffA);
;     if (wr == 1) PG8_BAR;
;     PG8_WAIT_V(2); PG8_BAR;
;     PG8_STAGE(PG8_SB(1, 0), cB + kstep, voffB); PG8_STAGE(PG8_SA(1, 0), cA + kstep, voffA); PG8_STAGE(PG8_SB(1, 1), cB + hstepB + kstep, voffB);
;     PG8_WAIT_V(6); PG8_BAR;
; __device__ __forceinline__ void cvt_load(const CvtState& cs, int lane, f32x4 (&v)[8]) {
;     const int kb = cs.next % CV_KB, tmp = cs.next / CV_KB, nb = tmp % CV_NB, e = tmp / CV_NB;
;     const float* src = cs.W + ((size_t)e * FF + (size_t)(128 * kb + 8 * (lane >> 2))) * D + 16 * nb + 4 * (lane & 3);
; #pragma unroll
;     for (int i = 0; i < 8; ++i) v[i] = *(const f32x4*)(src + (size_t)i * D);
; }
; __device__ __forceinline__ void cvt_store(CvtState& cs, int lane, const f32x4 (&v)[8]) {
;     const int kb = cs.next % CV_KB, tmp = cs.next / CV_KB, nb = tmp % CV_NB, e = tmp / CV_NB;
;     unsigned char* dst = cs.WT + ((size_t)e * D + (size_t)(16 * nb + 4 * (lane & 3))) * FF + 128 * kb + 8 * (lane >> 2);
; __global__ void __launch_bounds__(NTHREADS, 2) fwd_kernel(Args args) {
;     ...
;     if (PH(19)) RP(19)
;     {
;         LAS int* tlds = (LAS int*)(lds + LDSCTL_OFF + 1024);
;         { IDS(); if (tid < 256) tlds[tid] = TILE[tid]; __syncthreads(); }
;         const int ntiles = tlds[255];
;         pg8::Gemm g{(const bf16_t*)(ws + A_BUF), (const bf16_t*)(ws + W_MOEGU), D, D, D};
;         pg8::SchedMoe S; S.T.init(ntiles, 2 * FF / 256, G, bx); S.tile_e = tlds; S.atile = (size_t)256 * D; S.btile = (size_t)256 * D; S.nN = 2 * FF / 256;
;         pg8::EpiSwiglu<1> E{(void*)(ws + A_HM), FF, 1.0f / (WSC6 * ASC6), HSC8};
;         pg8::gemm_phase8<pg8::EpiSwiglu<1>, pg8::SchedMoe, 1>(lds, g, S, E);
.LBB0_1400:
	s_or_b64 exec, exec, s[4:5]
	v_readlane_b32 s98, v251, 9
	v_readlane_b32 s100, v251, 0
	v_readlane_b32 s101, v251, 1
	v_mbcnt_lo_u32_b32 v244, -1, 0
	v_mbcnt_hi_u32_b32 v244, -1, v244
	s_nop 3
	s_sub_u32 s100, s100, 0x28
	s_subb_u32 s101, s101, 0
	s_load_dwordx2 s[100:101], s[100:101], 0x0
	s_lshr_b32 s4, s98, 8
	s_lshr_b32 s5, s98, 1
	s_and_b32 s5, s5, 0x7f
	s_and_b32 s8, s98, 1
	s_mul_i32 s8, s8, 0xe00
	s_mul_i32 s9, s4, 0x1c00
	s_add_u32 s9, s9, s8
	s_lshl_b32 s9, s9, 13
	s_lshl_b32 s12, s5, 6
	s_add_u32 s9, s9, s12
	s_lshl_b32 s12, s4, 11
	s_lshl_b32 s13, s5, 4
	s_add_u32 s12, s12, s13
	s_mul_i32 s12, s12, 0x1c00
	s_add_u32 s12, s12, s8
	v_lshrrev_b32_e32 v245, 2, v244
	v_and_b32_e32 v246, 3, v244
	v_lshlrev_b32_e32 v247, 16, v245
	v_lshl_add_u32 v247, v246, 4, v247
	v_mul_u32_u24_e32 v246, 0x7000, v246
	v_lshl_add_u32 v246, v245, 3, v246
	v_add_u32_e32 v247, s9, v247
	v_add_u32_e32 v246, s12, v246
	s_add_u32 s4, s70, 0x24a00000
	s_addc_u32 s5, s71, 0
	s_waitcnt lgkmcnt(0)
	v_mov_b32_e32 v244, s100
	v_mov_b32_e32 v245, s101
	v_add_co_u32_e32 v244, vcc, v244, v247
	s_nop 1
	v_addc_co_u32_e32 v245, vcc, 0, v245, vcc
	v_mov_b32_e32 v247, s5
	v_add_co_u32_e32 v246, vcc, s4, v246
	s_nop 1
	v_addc_co_u32_e32 v247, vcc, 0, v247, vcc
	v_mov_b32_e32 v248, 0x43e00000
	v_mov_b32_e32 v249, 0xc3e00000
	s_mov_b32 s98, 14
	s_mov_b32 s99, 0
	s_mov_b32 s100, 0
	s_mov_b32 s101, 0
	s_add_u32 s8, s70, 0x3f200000
	s_addc_u32 s9, s71, 0
	s_cmp_lt_i32 s0, 0
	s_cselect_b64 s[12:13], -1, 0
	s_add_i32 s4, 0, 0x217fc
	v_mov_b32_e32 v1, s4
	s_waitcnt lgkmcnt(0)
	s_barrier
	ds_read_b32 v1, v1
	v_mov_b32_e32 v12, v0
	s_waitcnt lgkmcnt(0)
	v_mul_lo_u32 v154, v1, 56
	v_cmp_ge_i32_e32 vcc, s2, v154
	v_readfirstlane_b32 s24, v1
	v_readfirstlane_b32 s4, v12
	s_cbranch_vccnz .LBB0_1416
	v_lshlrev_b32_e32 v1, 4, v12
	v_add_u32_e32 v2, 0x2000, v1
	s_ashr_i32 s16, s4, 6
	v_ashrrev_i32_e32 v10, 7, v2
	v_bfe_u32 v4, v2, 7, 2
	s_mov_b32 s14, 0x1fffe0
	s_mul_i32 s25, s24, 7
	s_ashr_i32 s5, s4, 8
	s_lshl_b32 s17, s16, 10
	v_and_or_b32 v4, v10, s14, v4
	v_bfe_u32 v11, v2, 7, 4
	s_mov_b32 s14, 0x1ffff0
	v_ashrrev_i32_e32 v13, 3, v12
	v_bfe_u32 v14, v1, 7, 4
	s_add_i32 s33, s25, 1
	v_and_or_b32 v6, v10, s14, v11
	v_and_or_b32 v7, v13, s14, v14
	s_and_b64 s[14:15], s[12:13], exec
	s_cselect_b32 s14, s33, s25
	s_mul_i32 s14, s14, s0
	s_add_i32 s14, s14, s1
	v_lshrrev_b32_e32 v3, 7, v2
	v_lshrrev_b32_e32 v5, 2, v10
	v_lshrrev_b32_e32 v2, 6, v2
	s_mul_hi_i32 s15, s14, 0x92492493
	v_and_b32_e32 v5, 4, v5
	v_and_b32_e32 v2, 24, v2
	s_add_i32 s15, s15, s14
	v_or3_b32 v2, v4, v5, v2
	v_bfe_u32 v4, v3, 3, 1
	s_lshr_b32 s18, s15, 31
	s_ashr_i32 s15, s15, 8
	v_and_or_b32 v3, v3, 6, v4
	s_add_i32 s15, s15, s18
	v_lshlrev_b32_e32 v2, 11, v2
	v_lshlrev_b32_e32 v3, 4, v3
	v_and_b32_e32 v4, 0x70, v1
	s_lshl_b32 s18, s15, 3
	v_bitop3_b32 v156, v2, v3, v4 bitop3:0xf6
	v_lshlrev_b32_e32 v2, 11, v6
	s_sub_i32 s19, s24, s18
	v_bitop3_b32 v158, v3, v2, v4 bitop3:0xde
	v_bfe_u32 v2, v12, 3, 25
	v_and_b32_e32 v5, 0x1fffe0, v13
	v_lshrrev_b32_e32 v6, 2, v13
	v_lshrrev_b32_e32 v8, 2, v12
	s_min_i32 s19, s19, 8
	v_and_or_b32 v5, v2, 3, v5
	v_and_b32_e32 v6, 4, v6
	v_and_b32_e32 v8, 24, v8
	s_abs_i32 s20, s19
	v_or3_b32 v5, v5, v6, v8
	v_cvt_f32_u32_e32 v6, s20
	s_sub_i32 s22, 0, s20
	s_mulk_i32 s15, 0x1c0
	s_sub_i32 s14, s14, s15
	v_rcp_iflag_f32_e32 v6, v6
	s_abs_i32 s21, s14
	s_xor_b32 s15, s14, s19
	s_ashr_i32 s15, s15, 31
	v_mul_f32_e32 v6, 0x4f7ffffe, v6
	v_cvt_u32_f32_e32 v6, v6
	v_bfe_u32 v8, v2, 3, 1
	v_and_or_b32 v2, v2, 6, v8
	v_lshlrev_b32_e32 v5, 11, v5
	v_readfirstlane_b32 s23, v6
	s_mul_i32 s22, s22, s23
	s_mul_hi_u32 s22, s23, s22
	s_add_i32 s23, s23, s22
	s_mul_hi_u32 s22, s21, s23
	s_mul_i32 s23, s22, s20
	s_sub_i32 s21, s21, s23
	s_add_i32 s23, s22, 1
	s_sub_i32 s26, s21, s20
	s_cmp_ge_u32 s21, s20
	s_cselect_b32 s22, s23, s22
	s_cselect_b32 s21, s26, s21
	s_add_i32 s23, s22, 1
	s_cmp_ge_u32 s21, s20
	s_cselect_b32 s20, s23, s22
	s_xor_b32 s20, s20, s15
	s_sub_i32 s67, s20, s15
	s_mul_i32 s15, s67, s19
	s_sub_i32 s14, s14, s15
	s_add_i32 s42, s18, s14
	s_lshl_b32 s14, s42, 2
	s_add_i32 s14, s14, 0
	s_add_i32 s14, s14, 0x21400
	v_mov_b32_e32 v6, s14
	ds_read_b32 v6, v6
	s_ashr_i32 s15, s67, 31
	v_readlane_b32 s20, v251, 46
	v_lshlrev_b32_e32 v2, 4, v2
	v_bitop3_b32 v160, v5, v2, v4 bitop3:0xf6
	s_waitcnt lgkmcnt(0)
	v_readfirstlane_b32 s14, v6
	s_and_b32 s14, s14, 7
	s_mul_i32 s14, s14, 56
	s_add_u32 s14, s14, s67
	s_addc_u32 s15, 0, s15
	s_ashr_i32 s43, s42, 31
	s_lshl_b64 s[14:15], s[14:15], 19
	s_lshl_b64 s[18:19], s[42:43], 19
	s_add_u32 s46, s20, s14
	v_readlane_b32 s14, v251, 45
	s_addc_u32 s47, s14, s15
	s_add_i32 s35, s17, 0
	s_add_i32 s43, s35, 0x10000
	s_add_i32 s52, s35, 0x12000
	s_mov_b32 m0, s43
	s_add_u32 s14, s46, 0x40000
	global_load_lds_dwordx4 v160, s[46:47]
	s_mov_b32 m0, s52
	s_addc_u32 s15, s47, 0
	s_add_i32 s53, s35, 0x14000
	s_add_i32 s54, s35, 0x16000
	global_load_lds_dwordx4 v156, s[46:47]
	s_mov_b32 m0, s53
	s_add_u32 s44, s36, s18
	v_lshlrev_b32_e32 v5, 11, v7
	global_load_lds_dwordx4 v160, s[14:15]
	s_mov_b32 m0, s54
	s_addc_u32 s45, s37, s19
	s_add_i32 s55, s35, 0x2000
	v_bitop3_b32 v162, v2, v5, v4 bitop3:0xde
	global_load_lds_dwordx4 v156, s[14:15]
	s_mov_b32 m0, s35
	s_add_u32 s14, s44, 0x40000
	global_load_lds_dwordx4 v162, s[44:45]
	s_mov_b32 m0, s55
	s_addc_u32 s15, s45, 0
	s_add_i32 s56, s35, 0x4000
	global_load_lds_dwordx4 v158, s[44:45]
	s_mov_b32 m0, s56
	s_add_i32 s57, s35, 0x6000
	global_load_lds_dwordx4 v162, s[14:15]
	s_mov_b32 m0, s57
	v_mov_b32_e32 v161, 0
	global_load_lds_dwordx4 v158, s[14:15]
	s_movk_i32 s14, 0x70
	v_mov_b32_e32 v157, v161
	v_mov_b32_e32 v163, v161
	v_mov_b32_e32 v159, v161
	s_cmp_eq_u32 s5, 1
	v_bitop3_b32 v15, v3, v1, s14 bitop3:0x78
	v_bitop3_b32 v16, v2, v1, s14 bitop3:0x78
	v_lshl_add_u64 v[8:9], s[46:47], 0, v[160:161]
	v_lshl_add_u64 v[6:7], s[46:47], 0, v[156:157]
	v_lshl_add_u64 v[2:3], s[44:45], 0, v[162:163]
	s_cselect_b64 s[14:15], -1, 0
	s_cmp_lg_u32 s5, 1
	v_lshl_add_u64 v[4:5], s[44:45], 0, v[158:159]
	s_cbranch_scc1 .LBB0_1403
	s_barrier
